# pipelined attention + static s_setprio 1 for waves 4-7 during the tile loop
# baseline (speedup 1.0000x reference)
.LBB0_733:
	s_or_b64 exec, exec, s[8:9]
	s_movk_i32 s4, 0xf0
	s_cmp_lg_u32 0, -1
	v_lshlrev_b32_e32 v39, 8, v141
	v_bitop3_b32 v80, v142, s4, v136 bitop3:0x48
	s_cselect_b32 s10, 0, 0
	v_cvt_pk_bf16_f32 v96, v134, v135
	v_cvt_pk_bf16_f32 v97, v132, v133
	v_cvt_pk_bf16_f32 v98, v130, v131
	v_cvt_pk_bf16_f32 v99, v128, v129
	v_cvt_pk_bf16_f32 v100, v126, v127
	v_cvt_pk_bf16_f32 v101, v124, v125
	v_cvt_pk_bf16_f32 v102, v122, v123
	v_cvt_pk_bf16_f32 v103, v120, v121
	v_cvt_pk_bf16_f32 v104, v70, v71
	v_cvt_pk_bf16_f32 v105, v74, v75
	v_cvt_pk_bf16_f32 v106, v64, v65
	v_cvt_pk_bf16_f32 v107, v68, v69
	v_cvt_pk_bf16_f32 v108, v60, v61
	v_cvt_pk_bf16_f32 v109, v66, v67
	v_cvt_pk_bf16_f32 v110, v56, v57
	v_cvt_pk_bf16_f32 v111, v58, v59
	v_cvt_pk_bf16_f32 v112, v112, v113
	v_cvt_pk_bf16_f32 v113, v118, v119
	v_cvt_pk_bf16_f32 v114, v114, v115
	v_cvt_pk_bf16_f32 v115, v116, v117
	v_cvt_pk_bf16_f32 v116, v78, v79
	v_cvt_pk_bf16_f32 v117, v76, v77
	v_cvt_pk_bf16_f32 v118, v72, v73
	v_cvt_pk_bf16_f32 v119, v62, v63
	v_cvt_pk_bf16_f32 v120, v52, v53
	v_cvt_pk_bf16_f32 v121, v54, v55
	v_cvt_pk_bf16_f32 v122, v46, v47
	v_cvt_pk_bf16_f32 v123, v50, v51
	v_cvt_pk_bf16_f32 v124, v44, v45
	v_cvt_pk_bf16_f32 v125, v48, v49
	v_cvt_pk_bf16_f32 v126, v40, v41
	v_cvt_pk_bf16_f32 v127, v42, v43
	v_readlane_b32 s100, v250, 8
	v_mbcnt_lo_u32_b32 v68, -1, 0
	v_mbcnt_hi_u32_b32 v68, -1, v68
	s_nop 1
	v_add_u32_e32 v69, s100, v68
	v_lshrrev_b32_e32 v70, 3, v69
	v_and_b32_e32 v71, 7, v69
	v_lshrrev_b32_e32 v72, 2, v71
	v_bfe_u32 v73, v71, 1, 1
	v_and_b32_e32 v74, 1, v71
	v_lshlrev_b32_e32 v74, 1, v74
	v_lshl_add_u32 v75, v72, 2, v74
	v_bfe_u32 v76, v70, 1, 3
	v_xor_b32_e32 v77, v75, v76
	v_add_u32_e32 v78, 1, v75
	v_xor_b32_e32 v78, v78, v76
	v_lshlrev_b32_e32 v79, 7, v70
	v_lshl_add_u32 v79, v73, 3, v79
	v_lshl_add_u32 v64, v77, 4, v79
	v_lshl_add_u32 v65, v78, 4, v79
	v_add_u32_e32 v66, 0x2000, v64
	v_add_u32_e32 v67, 0x2000, v65
	v_or_b32_e32 v81, v39, v80
	s_add_i32 s15, s10, 0x10000
	v_and_b32_e32 v82, 6, v137
	v_lshrrev_b32_e32 v84, 4, v136
	s_waitcnt vmcnt(0)
	s_waitcnt vmcnt(0)
	s_add_i32 s11, s10, 0x12000
	v_lshl_add_u32 v83, v139, 7, s10
	v_bitop3_b32 v85, v84, v82, 7 bitop3:0x6c
	v_and_b32_e32 v86, 8, v138
	v_or_b32_e32 v82, 1, v82
	v_add_u32_e32 v225, s15, v81
	s_waitcnt vmcnt(4)
	ds_write_b128 v225, v[24:27] offset:0
	v_lshlrev_b32_e32 v85, 4, v85
	v_add_u32_e32 v87, v83, v86
	v_bitop3_b32 v82, v84, v82, 7 bitop3:0x6c
	v_add3_u32 v226, v80, s11, v39
	ds_write_b128 v226, v[28:31] offset:0
	v_lshlrev_b32_e32 v82, 4, v82
	v_add_u32_e32 v227, v87, v85
	ds_write_b64 v64, v[12:13] offset:0
	v_lshrrev_b32_e32 v32, 5, v136
	v_add_u32_e32 v83, 0x2000, v83
	v_or_b32_e32 v84, v85, v86
	v_add_u32_e32 v228, v87, v82
	ds_write_b64 v65, v[14:15] offset:0
	v_xor_b32_e32 v32, v32, v137
	v_or_b32_e32 v86, v82, v86
	v_add_u32_e32 v229, v84, v83
	ds_write_b64 v66, v[4:5] offset:0
	v_lshlrev_b32_e32 v32, 4, v32
	v_add_u32_e32 v184, v86, v83
	ds_write_b64 v67, v[6:7] offset:0
	v_lshlrev_b32_e32 v33, 8, v143
	v_and_b32_e32 v32, 16, v32
	v_bfe_u32 v35, v137, 1, 3
	s_waitcnt vmcnt(4)
	ds_write_b128 v225, v[20:23] offset:0x4000
	v_lshlrev_b32_e32 v36, 5, v35
	v_add3_u32 v32, v33, s15, v32
	s_movk_i32 s16, 0x60
	ds_write_b128 v226, v[16:19] offset:0x4000
	v_xad_u32 v204, v36, s16, v32
	s_movk_i32 s16, 0x80
	ds_write_b64 v64, v[8:9] offset:0x4000
	v_xad_u32 v205, v36, s16, v32
	s_movk_i32 s16, 0xa0
	ds_write_b64 v65, v[10:11] offset:0x4000
	s_add_u32 s8, s6, 0x100
	v_xad_u32 v206, v36, s16, v32
	s_movk_i32 s16, 0xc0
	ds_write_b64 v66, v[0:1] offset:0x4000
	s_addc_u32 s9, s7, 0
	v_xad_u32 v207, v36, s16, v32
	s_movk_i32 s16, 0xe0
	ds_write_b64 v67, v[2:3] offset:0x4000
	v_add_u32_e32 v201, v32, v36
	v_xad_u32 v202, v36, 32, v32
	v_xad_u32 v203, v36, 64, v32
	v_xad_u32 v208, v36, s16, v32
	v_lshl_add_u32 v32, v143, 7, s10
	s_add_u32 s10, s78, 0x20000
	global_load_dwordx4 v[132:135], v198, s[8:9]
	s_addc_u32 s11, s79, 0
	global_load_dwordx4 v[128:131], v199, s[8:9]
	v_lshrrev_b32_e32 v34, 1, v137
	global_load_dwordx4 v[136:139], v196, s[10:11]
	s_add_u32 s6, s6, 0x180
	v_bitop3_b32 v34, v140, v34, 7 bitop3:0x78
	v_bitop3_b32 v37, v140, v35, 2 bitop3:0x36
	v_bitop3_b32 v38, v140, v35, 4 bitop3:0x36
	v_bitop3_b32 v35, v140, v35, 6 bitop3:0x36
	global_load_dwordx4 v[140:143], v197, s[10:11]
	s_addc_u32 s7, s7, 0
	s_add_u32 s8, s78, 0x30000
	global_load_dwordx4 v[148:151], v198, s[6:7]
	s_addc_u32 s9, s79, 0
	global_load_dwordx4 v[144:147], v199, s[6:7]
	global_load_dwordx4 v[152:155], v196, s[8:9]
	s_add_u32 s10, s13, s14
	global_load_dwordx4 v[156:159], v197, s[8:9]
	s_addc_u32 s11, s12, 0
	s_add_u32 s12, s41, s30
	v_mov_b32_e32 v0, 0
	s_mov_b32 s4, 0
	v_lshl_add_u32 v209, v34, 4, v32
	v_lshl_add_u32 v210, v37, 4, v32
	v_lshl_add_u32 v211, v38, 4, v32
	v_lshl_add_u32 v224, v35, 4, v32
	s_addc_u32 s13, 0, s31
	v_mov_b32_e32 v1, v0
	v_mov_b32_e32 v2, v0
	v_mov_b32_e32 v3, v0
	v_mov_b32_e32 v4, v0
	v_mov_b32_e32 v5, v0
	v_mov_b32_e32 v6, v0
	v_mov_b32_e32 v7, v0
	v_mov_b32_e32 v8, v0
	v_mov_b32_e32 v9, v0
	v_mov_b32_e32 v10, v0
	v_mov_b32_e32 v11, v0
	v_mov_b32_e32 v12, v0
	v_mov_b32_e32 v13, v0
	v_mov_b32_e32 v14, v0
	v_mov_b32_e32 v15, v0
	v_mov_b32_e32 v16, v0
	v_mov_b32_e32 v17, v0
	v_mov_b32_e32 v18, v0
	v_mov_b32_e32 v19, v0
	v_mov_b32_e32 v20, v0
	v_mov_b32_e32 v21, v0
	v_mov_b32_e32 v22, v0
	v_mov_b32_e32 v23, v0
	v_mov_b32_e32 v24, v0
	v_mov_b32_e32 v25, v0
	v_mov_b32_e32 v26, v0
	v_mov_b32_e32 v27, v0
	v_mov_b32_e32 v28, v0
	v_mov_b32_e32 v29, v0
	v_mov_b32_e32 v30, v0
	v_mov_b32_e32 v31, v0
	v_mov_b32_e32 v32, v0
	v_mov_b32_e32 v33, v0
	v_mov_b32_e32 v34, v0
	v_mov_b32_e32 v35, v0
	v_mov_b32_e32 v36, v0
	v_mov_b32_e32 v37, v0
	v_mov_b32_e32 v38, v0
	v_mov_b32_e32 v39, v0
	v_mov_b32_e32 v40, v0
	v_mov_b32_e32 v41, v0
	v_mov_b32_e32 v42, v0
	v_mov_b32_e32 v43, v0
	v_mov_b32_e32 v44, v0
	v_mov_b32_e32 v45, v0
	v_mov_b32_e32 v46, v0
	v_mov_b32_e32 v47, v0
	v_mov_b32_e32 v48, v0
	v_mov_b32_e32 v49, v0
	v_mov_b32_e32 v50, v0
	v_mov_b32_e32 v51, v0
	v_mov_b32_e32 v52, v0
	v_mov_b32_e32 v53, v0
	v_mov_b32_e32 v54, v0
	v_mov_b32_e32 v55, v0
	v_mov_b32_e32 v56, v0
	v_mov_b32_e32 v57, v0
	v_mov_b32_e32 v58, v0
	v_mov_b32_e32 v59, v0
	v_mov_b32_e32 v60, v0
	v_mov_b32_e32 v61, v0
	v_mov_b32_e32 v62, v0
	v_mov_b32_e32 v63, v0
	v_mov_b32_e32 v160, v0
	v_mov_b32_e32 v161, v0
	v_mov_b32_e32 v227, v64
	v_mov_b32_e32 v228, v65
	v_mov_b32_e32 v229, v66
	v_mov_b32_e32 v184, v67
	v_readlane_b32 s100, v250, 8
	v_mbcnt_lo_u32_b32 v68, -1, 0
	v_mbcnt_hi_u32_b32 v68, -1, v68
	v_and_b32_e32 v69, 15, v68
	v_lshrrev_b32_e32 v70, 4, v68
	v_lshlrev_b32_e32 v72, 8, v69
	v_add_u32_e32 v72, 0x10000, v72
	v_add_u32_e32 v71, 0, v70
	v_xor_b32_e32 v71, v71, v69
	v_lshl_add_u32 v201, v71, 4, v72
	v_add_u32_e32 v71, 4, v70
	v_xor_b32_e32 v71, v71, v69
	v_lshl_add_u32 v202, v71, 4, v72
	v_add_u32_e32 v71, 8, v70
	v_xor_b32_e32 v71, v71, v69
	v_lshl_add_u32 v203, v71, 4, v72
	v_add_u32_e32 v71, 12, v70
	v_xor_b32_e32 v71, v71, v69
	v_lshl_add_u32 v246, v71, 4, v72
	v_bfe_u32 v73, v69, 1, 3
	v_lshlrev_b32_e32 v76, 7, v69
	v_add_u32_e32 v71, 0, v70
	v_xor_b32_e32 v71, v71, v73
	v_lshl_add_u32 v209, v71, 4, v76
	v_add_u32_e32 v71, 4, v70
	v_xor_b32_e32 v71, v71, v73
	v_lshl_add_u32 v210, v71, 4, v76
	s_lshl_b32 s101, s100, 7
	s_add_u32 s101, s101, 0x8000
	s_cmpk_ge_u32 s100, 0x100
	s_cselect_b32 s6, 0x8000, 0
	s_add_u32 s101, s101, s6
	v_and_b32_e32 v74, 31, v68
	v_lshrrev_b32_e32 v75, 5, v68
	v_lshlrev_b32_e32 v74, 8, v74
	v_lshl_add_u32 v74, v75, 4, v74
	v_add_u32_e32 v74, s101, v74
	v_lshlrev_b32_e32 v75, 8, v69
	v_lshl_add_u32 v75, v70, 4, v75
	v_add_u32_e32 v75, s101, v75
	ds_write_b128 v74, v[96:99] offset:0
	ds_write_b128 v74, v[100:103] offset:32
	ds_write_b128 v74, v[104:107] offset:64
	ds_write_b128 v74, v[108:111] offset:96
	ds_write_b128 v74, v[112:115] offset:128
	ds_write_b128 v74, v[116:119] offset:160
	ds_write_b128 v74, v[120:123] offset:192
	ds_write_b128 v74, v[124:127] offset:224
	s_waitcnt lgkmcnt(0)
	ds_read_b128 v[96:99], v75 offset:0
	ds_read_b128 v[100:103], v75 offset:64
	ds_read_b128 v[104:107], v75 offset:128
	ds_read_b128 v[108:111], v75 offset:192
	ds_read_b128 v[112:115], v75 offset:4096
	ds_read_b128 v[116:119], v75 offset:4160
	ds_read_b128 v[120:123], v75 offset:4224
	ds_read_b128 v[124:127], v75 offset:4288
	s_waitcnt vmcnt(0)
	s_waitcnt lgkmcnt(0)
	s_barrier
	ds_write_b128 v225, v[136:139] offset:32768
	ds_write_b128 v226, v[140:143] offset:32768
	s_add_u32 s15, s22, s12
	s_addc_u32 s14, s23, s13
	s_add_u32 s6, s15, 0x23a40000
	s_addc_u32 s7, s14, 0
	s_waitcnt lgkmcnt(0)
	global_load_dwordx4 v[136:139], v196, s[6:7]
	global_load_dwordx4 v[140:143], v197, s[6:7]
	v_mov_b32_e32 v194, 0
	v_mov_b32_e32 v195, 0
	s_barrier
	s_cmpk_lt_u32 s100, 0x100
	s_cbranch_scc1 .Lattn_noprio
	s_setprio 1
.Lattn_noprio:
	ds_read_b128 v[160:163], v201 offset:0
	ds_read_b128 v[164:167], v202 offset:0
	ds_read_b128 v[168:171], v203 offset:0
	ds_read_b128 v[172:175], v246 offset:0
	ds_read_b128 v[176:179], v201 offset:4096
	ds_read_b128 v[180:183], v202 offset:4096
	ds_read_b128 v[230:233], v203 offset:4096
	s_waitcnt lgkmcnt(6)
	v_mfma_f32_16x16x32_bf16 v[64:67], v[160:163], v[96:99], 0
	v_mfma_f32_16x16x32_bf16 v[68:71], v[160:163], v[112:115], 0
	ds_read_b128 v[234:237], v246 offset:4096
	s_waitcnt lgkmcnt(6)
	v_mfma_f32_16x16x32_bf16 v[68:71], v[164:167], v[116:119], v[68:71]
	v_mfma_f32_16x16x32_bf16 v[64:67], v[164:167], v[100:103], v[64:67]
	ds_read_b128 v[160:163], v201 offset:8192
	s_waitcnt lgkmcnt(6)
	v_mfma_f32_16x16x32_bf16 v[64:67], v[168:171], v[104:107], v[64:67]
	v_mfma_f32_16x16x32_bf16 v[68:71], v[168:171], v[120:123], v[68:71]
	ds_read_b128 v[164:167], v202 offset:8192
	s_waitcnt lgkmcnt(6)
	v_mfma_f32_16x16x32_bf16 v[68:71], v[172:175], v[124:127], v[68:71]
	v_mfma_f32_16x16x32_bf16 v[64:67], v[172:175], v[108:111], v[64:67]
	ds_read_b128 v[168:171], v203 offset:8192
	s_waitcnt lgkmcnt(6)
	v_mfma_f32_16x16x32_bf16 v[72:75], v[176:179], v[96:99], 0
	s_nop 7
	s_nop 1
	v_exp_f32_e32 v64, v64
	v_exp_f32_e32 v68, v68
	v_mfma_f32_16x16x32_bf16 v[76:79], v[176:179], v[112:115], 0
	v_exp_f32_e32 v65, v65
	v_exp_f32_e32 v69, v69
	ds_read_b128 v[172:175], v246 offset:8192
	s_waitcnt lgkmcnt(6)
	v_mfma_f32_16x16x32_bf16 v[76:79], v[180:183], v[116:119], v[76:79]
	v_exp_f32_e32 v66, v66
	v_exp_f32_e32 v70, v70
	v_mfma_f32_16x16x32_bf16 v[72:75], v[180:183], v[100:103], v[72:75]
	v_exp_f32_e32 v67, v67
	v_exp_f32_e32 v71, v71
	ds_read_b128 v[176:179], v201 offset:12288
	s_waitcnt lgkmcnt(6)
	v_mfma_f32_16x16x32_bf16 v[72:75], v[230:233], v[104:107], v[72:75]
	v_add_f32_e32 v220, v64, v65
	v_add_f32_e32 v221, v68, v69
	v_mfma_f32_16x16x32_bf16 v[76:79], v[230:233], v[120:123], v[76:79]
	v_add_f32_e32 v220, v220, v66
	v_add_f32_e32 v221, v221, v70
	ds_read_b128 v[180:183], v202 offset:12288
	s_waitcnt lgkmcnt(6)
	v_mfma_f32_16x16x32_bf16 v[76:79], v[234:237], v[124:127], v[76:79]
	v_add_f32_e32 v220, v220, v67
	v_mfma_f32_16x16x32_bf16 v[72:75], v[234:237], v[108:111], v[72:75]
	v_add_f32_e32 v221, v221, v71
	ds_read_b128 v[230:233], v203 offset:12288
	s_waitcnt lgkmcnt(6)
	v_mfma_f32_16x16x32_bf16 v[80:83], v[160:163], v[96:99], 0
	s_nop 7
	s_nop 1
	v_exp_f32_e32 v72, v72
	v_exp_f32_e32 v76, v76
	v_exp_f32_e32 v73, v73
	v_mfma_f32_16x16x32_bf16 v[84:87], v[160:163], v[112:115], 0
	v_exp_f32_e32 v77, v77
	v_exp_f32_e32 v74, v74
	v_exp_f32_e32 v78, v78
	ds_read_b128 v[234:237], v246 offset:12288
	s_waitcnt lgkmcnt(6)
	v_mfma_f32_16x16x32_bf16 v[84:87], v[164:167], v[116:119], v[84:87]
	v_exp_f32_e32 v75, v75
	v_exp_f32_e32 v79, v79
	v_add_f32_e32 v220, v220, v72
	v_mfma_f32_16x16x32_bf16 v[80:83], v[164:167], v[100:103], v[80:83]
	v_add_f32_e32 v221, v221, v76
	v_add_f32_e32 v220, v220, v73
	v_add_f32_e32 v221, v221, v77
	s_waitcnt lgkmcnt(5)
	v_mfma_f32_16x16x32_bf16 v[80:83], v[168:171], v[104:107], v[80:83]
	v_add_f32_e32 v220, v220, v74
	v_add_f32_e32 v221, v221, v78
	v_add_f32_e32 v220, v220, v75
	v_mfma_f32_16x16x32_bf16 v[84:87], v[168:171], v[120:123], v[84:87]
	v_add_f32_e32 v221, v221, v79
	v_cvt_pk_bf16_f32 v216, v64, v65
	v_cvt_pk_bf16_f32 v217, v66, v67
	s_waitcnt lgkmcnt(4)
	v_mfma_f32_16x16x32_bf16 v[84:87], v[172:175], v[124:127], v[84:87]
	v_cvt_pk_bf16_f32 v238, v68, v69
	v_cvt_pk_bf16_f32 v239, v70, v71
	v_cvt_pk_bf16_f32 v218, v72, v73
	v_mfma_f32_16x16x32_bf16 v[80:83], v[172:175], v[108:111], v[80:83]
	v_cvt_pk_bf16_f32 v219, v74, v75
	v_cvt_pk_bf16_f32 v240, v76, v77
	v_cvt_pk_bf16_f32 v241, v78, v79
	s_waitcnt lgkmcnt(3)
	v_mfma_f32_16x16x32_bf16 v[88:91], v[176:179], v[96:99], 0
	s_nop 7
	s_nop 1
	v_exp_f32_e32 v80, v80
	v_exp_f32_e32 v84, v84
	v_mfma_f32_16x16x32_bf16 v[92:95], v[176:179], v[112:115], 0
	v_exp_f32_e32 v81, v81
	v_exp_f32_e32 v85, v85
	s_waitcnt lgkmcnt(2)
	v_mfma_f32_16x16x32_bf16 v[92:95], v[180:183], v[116:119], v[92:95]
	v_exp_f32_e32 v82, v82
	v_exp_f32_e32 v86, v86
	v_mfma_f32_16x16x32_bf16 v[88:91], v[180:183], v[100:103], v[88:91]
	v_exp_f32_e32 v83, v83
	v_exp_f32_e32 v87, v87
	s_waitcnt lgkmcnt(1)
	v_mfma_f32_16x16x32_bf16 v[88:91], v[230:233], v[104:107], v[88:91]
	v_add_f32_e32 v220, v220, v80
	v_add_f32_e32 v221, v221, v84
	v_mfma_f32_16x16x32_bf16 v[92:95], v[230:233], v[120:123], v[92:95]
	v_add_f32_e32 v220, v220, v81
	v_add_f32_e32 v221, v221, v85
	s_waitcnt lgkmcnt(0)
	v_mfma_f32_16x16x32_bf16 v[92:95], v[234:237], v[124:127], v[92:95]
	v_add_f32_e32 v220, v220, v82
	v_add_f32_e32 v221, v221, v86
	v_mfma_f32_16x16x32_bf16 v[88:91], v[234:237], v[108:111], v[88:91]
	v_add_f32_e32 v220, v220, v83
	v_add_f32_e32 v221, v221, v87
.LBB0_734:
	s_waitcnt lgkmcnt(0)
	s_barrier
	ds_read_b128 v[160:163], v201 offset:16384
	ds_read_b128 v[164:167], v209 offset:0
	ds_read_b128 v[168:171], v202 offset:16384
	ds_read_b128 v[172:175], v209 offset:2048
	ds_read_b128 v[176:179], v203 offset:16384
	ds_read_b128 v[180:183], v209 offset:4096
	ds_read_b128 v[230:233], v246 offset:16384
	s_waitcnt lgkmcnt(6)
	v_mfma_f32_16x16x32_bf16 v[64:67], v[160:163], v[96:99], 0
	v_exp_f32_e32 v88, v88
	v_exp_f32_e32 v92, v92
	v_mfma_f32_16x16x32_bf16 v[68:71], v[160:163], v[112:115], 0
	v_cvt_pk_bf16_f32 v242, v80, v81
	v_exp_f32_e32 v89, v89
	ds_read_b128 v[234:237], v209 offset:6144
	s_add_u32 s16, s22, s10
	s_addc_u32 s17, s23, s11
	s_add_u32 s15, s22, s12
	s_addc_u32 s14, s23, s13
	s_add_u32 s8, s16, 0x3bc00200
	s_addc_u32 s9, s17, 0
	s_add_u32 s6, s15, 0x23a50000
	s_addc_u32 s7, s14, 0
	s_waitcnt lgkmcnt(6)
	v_mfma_f32_16x16x32_bf16 v[0:3], v[164:167], v[216:219], v[0:3]
	v_exp_f32_e32 v93, v93
	v_cvt_pk_bf16_f32 v243, v82, v83
	v_mfma_f32_16x16x32_bf16 v[4:7], v[164:167], v[238:241], v[4:7]
	v_exp_f32_e32 v90, v90
	v_exp_f32_e32 v94, v94
	ds_read_b128 v[160:163], v201 offset:20480
	s_waitcnt vmcnt(4)
	ds_write_b128 v225, v[152:155] offset:49152
	s_waitcnt lgkmcnt(7)
	v_mfma_f32_16x16x32_bf16 v[68:71], v[168:171], v[116:119], v[68:71]
	v_cvt_pk_bf16_f32 v204, v84, v85
	v_mfma_f32_16x16x32_bf16 v[64:67], v[168:171], v[100:103], v[64:67]
	v_exp_f32_e32 v91, v91
	ds_read_b128 v[164:167], v209 offset:8192
	ds_write_b128 v226, v[156:159] offset:49152
	s_waitcnt lgkmcnt(8)
	v_mfma_f32_16x16x32_bf16 v[12:15], v[172:175], v[238:241], v[12:15]
	v_exp_f32_e32 v95, v95
	v_mfma_f32_16x16x32_bf16 v[8:11], v[172:175], v[216:219], v[8:11]
	v_cvt_pk_bf16_f32 v205, v86, v87
	ds_read_b128 v[168:171], v202 offset:20480
	ds_write_b64 v227, v[132:133] offset:32768
	s_waitcnt lgkmcnt(9)
	v_mfma_f32_16x16x32_bf16 v[64:67], v[176:179], v[104:107], v[64:67]
	v_add_f32_e32 v220, v220, v88
	v_mfma_f32_16x16x32_bf16 v[68:71], v[176:179], v[120:123], v[68:71]
	v_add_f32_e32 v221, v221, v92
	ds_read_b128 v[172:175], v209 offset:10240
	ds_write_b64 v228, v[134:135] offset:32768
	s_waitcnt lgkmcnt(10)
	v_mfma_f32_16x16x32_bf16 v[16:19], v[180:183], v[216:219], v[16:19]
	v_add_f32_e32 v220, v220, v89
	v_mfma_f32_16x16x32_bf16 v[20:23], v[180:183], v[238:241], v[20:23]
	v_add_f32_e32 v221, v221, v93
	ds_read_b128 v[176:179], v203 offset:20480
	ds_write_b64 v229, v[128:129] offset:32768
	s_waitcnt lgkmcnt(11)
	v_mfma_f32_16x16x32_bf16 v[68:71], v[230:233], v[124:127], v[68:71]
	v_cvt_pk_bf16_f32 v244, v88, v89
	v_mfma_f32_16x16x32_bf16 v[64:67], v[230:233], v[108:111], v[64:67]
	v_cvt_pk_bf16_f32 v245, v90, v91
	ds_read_b128 v[180:183], v209 offset:12288
	ds_write_b64 v184, v[130:131] offset:32768
	s_waitcnt lgkmcnt(12)
	v_mfma_f32_16x16x32_bf16 v[28:31], v[234:237], v[238:241], v[28:31]
	v_cvt_pk_bf16_f32 v206, v92, v93
	v_mfma_f32_16x16x32_bf16 v[24:27], v[234:237], v[216:219], v[24:27]
	v_cvt_pk_bf16_f32 v207, v94, v95
	ds_read_b128 v[230:233], v246 offset:20480
	global_load_dwordx4 v[132:135], v198, s[8:9]
	s_waitcnt lgkmcnt(12)
	v_mfma_f32_16x16x32_bf16 v[72:75], v[160:163], v[96:99], 0
	v_add_f32_e32 v220, v220, v90
	v_add_f32_e32 v221, v221, v94
	v_mfma_f32_16x16x32_bf16 v[76:79], v[160:163], v[112:115], 0
	v_add_f32_e32 v220, v220, v91
	v_add_f32_e32 v221, v221, v95
	ds_read_b128 v[234:237], v209 offset:14336
	global_load_dwordx4 v[128:131], v199, s[8:9]
	s_waitcnt lgkmcnt(11)
	v_mfma_f32_16x16x32_bf16 v[32:35], v[164:167], v[216:219], v[32:35]
	v_add_f32_e32 v194, v194, v220
	v_add_f32_e32 v195, v195, v221
	v_mfma_f32_16x16x32_bf16 v[36:39], v[164:167], v[238:241], v[36:39]
	v_exp_f32_e32 v64, v64
	v_exp_f32_e32 v68, v68
	ds_read_b128 v[160:163], v201 offset:24576
	global_load_dwordx4 v[152:155], v196, s[6:7]
	s_waitcnt lgkmcnt(10)
	v_mfma_f32_16x16x32_bf16 v[76:79], v[168:171], v[116:119], v[76:79]
	v_exp_f32_e32 v65, v65
	v_mfma_f32_16x16x32_bf16 v[72:75], v[168:171], v[100:103], v[72:75]
	v_exp_f32_e32 v69, v69
	ds_read_b128 v[164:167], v210 offset:0
	global_load_dwordx4 v[156:159], v197, s[6:7]
	s_waitcnt lgkmcnt(9)
	v_mfma_f32_16x16x32_bf16 v[44:47], v[172:175], v[238:241], v[44:47]
	v_exp_f32_e32 v66, v66
	v_mfma_f32_16x16x32_bf16 v[40:43], v[172:175], v[216:219], v[40:43]
	v_exp_f32_e32 v70, v70
	ds_read_b128 v[168:171], v202 offset:24576
	s_waitcnt lgkmcnt(8)
	v_mfma_f32_16x16x32_bf16 v[72:75], v[176:179], v[104:107], v[72:75]
	v_exp_f32_e32 v67, v67
	v_mfma_f32_16x16x32_bf16 v[76:79], v[176:179], v[120:123], v[76:79]
	v_exp_f32_e32 v71, v71
	ds_read_b128 v[172:175], v210 offset:2048
	s_waitcnt lgkmcnt(7)
	v_mfma_f32_16x16x32_bf16 v[48:51], v[180:183], v[216:219], v[48:51]
	v_add_f32_e32 v220, v64, v65
	v_mfma_f32_16x16x32_bf16 v[52:55], v[180:183], v[238:241], v[52:55]
	v_add_f32_e32 v221, v68, v69
	ds_read_b128 v[176:179], v203 offset:24576
	s_waitcnt lgkmcnt(6)
	v_mfma_f32_16x16x32_bf16 v[76:79], v[230:233], v[124:127], v[76:79]
	v_add_f32_e32 v220, v220, v66
	v_mfma_f32_16x16x32_bf16 v[72:75], v[230:233], v[108:111], v[72:75]
	v_add_f32_e32 v221, v221, v70
	ds_read_b128 v[180:183], v210 offset:4096
	s_waitcnt lgkmcnt(6)
	v_mfma_f32_16x16x32_bf16 v[60:63], v[234:237], v[238:241], v[60:63]
	v_add_f32_e32 v220, v220, v67
	v_mfma_f32_16x16x32_bf16 v[56:59], v[234:237], v[216:219], v[56:59]
	v_add_f32_e32 v221, v221, v71
	ds_read_b128 v[230:233], v246 offset:24576
	s_waitcnt lgkmcnt(6)
	v_mfma_f32_16x16x32_bf16 v[80:83], v[160:163], v[96:99], 0
	v_exp_f32_e32 v72, v72
	v_exp_f32_e32 v76, v76
	v_mfma_f32_16x16x32_bf16 v[84:87], v[160:163], v[112:115], 0
	v_exp_f32_e32 v73, v73
	v_exp_f32_e32 v77, v77
	ds_read_b128 v[234:237], v210 offset:6144
	s_waitcnt lgkmcnt(6)
	v_mfma_f32_16x16x32_bf16 v[0:3], v[164:167], v[242:245], v[0:3]
	v_exp_f32_e32 v74, v74
	v_exp_f32_e32 v78, v78
	v_mfma_f32_16x16x32_bf16 v[4:7], v[164:167], v[204:207], v[4:7]
	v_exp_f32_e32 v75, v75
	v_exp_f32_e32 v79, v79
	ds_read_b128 v[160:163], v201 offset:28672
	s_waitcnt lgkmcnt(6)
	v_mfma_f32_16x16x32_bf16 v[84:87], v[168:171], v[116:119], v[84:87]
	v_add_f32_e32 v220, v220, v72
	v_mfma_f32_16x16x32_bf16 v[80:83], v[168:171], v[100:103], v[80:83]
	v_add_f32_e32 v221, v221, v76
	ds_read_b128 v[164:167], v210 offset:8192
	s_waitcnt lgkmcnt(6)
	v_mfma_f32_16x16x32_bf16 v[12:15], v[172:175], v[204:207], v[12:15]
	v_add_f32_e32 v220, v220, v73
	v_mfma_f32_16x16x32_bf16 v[8:11], v[172:175], v[242:245], v[8:11]
	v_add_f32_e32 v221, v221, v77
	ds_read_b128 v[168:171], v202 offset:28672
	s_waitcnt lgkmcnt(6)
	v_mfma_f32_16x16x32_bf16 v[80:83], v[176:179], v[104:107], v[80:83]
	v_add_f32_e32 v220, v220, v74
	v_mfma_f32_16x16x32_bf16 v[84:87], v[176:179], v[120:123], v[84:87]
	v_add_f32_e32 v221, v221, v78
	ds_read_b128 v[172:175], v210 offset:10240
	s_waitcnt lgkmcnt(6)
	v_mfma_f32_16x16x32_bf16 v[16:19], v[180:183], v[242:245], v[16:19]
	v_add_f32_e32 v220, v220, v75
	v_mfma_f32_16x16x32_bf16 v[20:23], v[180:183], v[204:207], v[20:23]
	v_add_f32_e32 v221, v221, v79
	ds_read_b128 v[176:179], v203 offset:28672
	s_waitcnt lgkmcnt(6)
	v_mfma_f32_16x16x32_bf16 v[84:87], v[230:233], v[124:127], v[84:87]
	v_cvt_pk_bf16_f32 v216, v64, v65
	v_mfma_f32_16x16x32_bf16 v[80:83], v[230:233], v[108:111], v[80:83]
	v_cvt_pk_bf16_f32 v217, v66, v67
	ds_read_b128 v[180:183], v210 offset:12288
	s_waitcnt lgkmcnt(6)
	v_mfma_f32_16x16x32_bf16 v[28:31], v[234:237], v[204:207], v[28:31]
	v_cvt_pk_bf16_f32 v238, v68, v69
	v_mfma_f32_16x16x32_bf16 v[24:27], v[234:237], v[242:245], v[24:27]
	v_cvt_pk_bf16_f32 v239, v70, v71
	ds_read_b128 v[230:233], v246 offset:28672
	s_waitcnt lgkmcnt(6)
	v_mfma_f32_16x16x32_bf16 v[88:91], v[160:163], v[96:99], 0
	v_exp_f32_e32 v80, v80
	v_exp_f32_e32 v84, v84
	v_mfma_f32_16x16x32_bf16 v[92:95], v[160:163], v[112:115], 0
	v_exp_f32_e32 v81, v81
	v_exp_f32_e32 v85, v85
	ds_read_b128 v[234:237], v210 offset:14336
	s_waitcnt lgkmcnt(6)
	v_mfma_f32_16x16x32_bf16 v[32:35], v[164:167], v[242:245], v[32:35]
	v_exp_f32_e32 v82, v82
	v_exp_f32_e32 v86, v86
	v_mfma_f32_16x16x32_bf16 v[36:39], v[164:167], v[204:207], v[36:39]
	v_exp_f32_e32 v83, v83
	v_exp_f32_e32 v87, v87
	ds_read_b128 v[160:163], v201 offset:32768
	s_waitcnt lgkmcnt(6)
	v_mfma_f32_16x16x32_bf16 v[92:95], v[168:171], v[116:119], v[92:95]
	v_add_f32_e32 v220, v220, v80
	v_mfma_f32_16x16x32_bf16 v[88:91], v[168:171], v[100:103], v[88:91]
	v_add_f32_e32 v221, v221, v84
	ds_read_b128 v[164:167], v209 offset:16384
	s_waitcnt lgkmcnt(6)
	v_mfma_f32_16x16x32_bf16 v[44:47], v[172:175], v[204:207], v[44:47]
	v_add_f32_e32 v220, v220, v81
	v_mfma_f32_16x16x32_bf16 v[40:43], v[172:175], v[242:245], v[40:43]
	v_add_f32_e32 v221, v221, v85
	ds_read_b128 v[168:171], v202 offset:32768
	s_waitcnt lgkmcnt(6)
	v_mfma_f32_16x16x32_bf16 v[88:91], v[176:179], v[104:107], v[88:91]
	v_add_f32_e32 v220, v220, v82
	v_mfma_f32_16x16x32_bf16 v[92:95], v[176:179], v[120:123], v[92:95]
	v_add_f32_e32 v221, v221, v86
	ds_read_b128 v[172:175], v209 offset:18432
	s_waitcnt lgkmcnt(6)
	v_mfma_f32_16x16x32_bf16 v[48:51], v[180:183], v[242:245], v[48:51]
	v_add_f32_e32 v220, v220, v83
	v_mfma_f32_16x16x32_bf16 v[52:55], v[180:183], v[204:207], v[52:55]
	v_add_f32_e32 v221, v221, v87
	ds_read_b128 v[176:179], v203 offset:32768
	s_waitcnt lgkmcnt(6)
	v_mfma_f32_16x16x32_bf16 v[92:95], v[230:233], v[124:127], v[92:95]
	v_cvt_pk_bf16_f32 v218, v72, v73
	v_mfma_f32_16x16x32_bf16 v[88:91], v[230:233], v[108:111], v[88:91]
	v_cvt_pk_bf16_f32 v219, v74, v75
	ds_read_b128 v[180:183], v209 offset:20480
	s_waitcnt lgkmcnt(6)
	v_mfma_f32_16x16x32_bf16 v[60:63], v[234:237], v[204:207], v[60:63]
	v_cvt_pk_bf16_f32 v240, v76, v77
	v_mfma_f32_16x16x32_bf16 v[56:59], v[234:237], v[242:245], v[56:59]
	v_cvt_pk_bf16_f32 v241, v78, v79
	ds_read_b128 v[230:233], v246 offset:32768
	s_waitcnt lgkmcnt(6)
	v_mfma_f32_16x16x32_bf16 v[64:67], v[160:163], v[96:99], 0
	v_exp_f32_e32 v88, v88
	v_exp_f32_e32 v92, v92
	v_mfma_f32_16x16x32_bf16 v[68:71], v[160:163], v[112:115], 0
	v_cvt_pk_bf16_f32 v242, v80, v81
	v_exp_f32_e32 v89, v89
	ds_read_b128 v[234:237], v209 offset:22528
	s_add_u32 s8, s16, 0x3bc00280
	s_addc_u32 s9, s17, 0
	s_add_u32 s6, s15, 0x23a60000
	s_addc_u32 s7, s14, 0
	s_waitcnt lgkmcnt(6)
	v_mfma_f32_16x16x32_bf16 v[0:3], v[164:167], v[216:219], v[0:3]
	v_exp_f32_e32 v93, v93
	v_cvt_pk_bf16_f32 v243, v82, v83
	v_mfma_f32_16x16x32_bf16 v[4:7], v[164:167], v[238:241], v[4:7]
	v_exp_f32_e32 v90, v90
	v_exp_f32_e32 v94, v94
	ds_read_b128 v[160:163], v201 offset:36864
	s_waitcnt vmcnt(4)
	ds_write_b128 v225, v[136:139] offset:0
	s_waitcnt lgkmcnt(7)
	v_mfma_f32_16x16x32_bf16 v[68:71], v[168:171], v[116:119], v[68:71]
	v_cvt_pk_bf16_f32 v204, v84, v85
	v_mfma_f32_16x16x32_bf16 v[64:67], v[168:171], v[100:103], v[64:67]
	v_exp_f32_e32 v91, v91
	ds_read_b128 v[164:167], v209 offset:24576
	ds_write_b128 v226, v[140:143] offset:0
	s_waitcnt lgkmcnt(8)
	v_mfma_f32_16x16x32_bf16 v[12:15], v[172:175], v[238:241], v[12:15]
	v_exp_f32_e32 v95, v95
	v_mfma_f32_16x16x32_bf16 v[8:11], v[172:175], v[216:219], v[8:11]
	v_cvt_pk_bf16_f32 v205, v86, v87
	ds_read_b128 v[168:171], v202 offset:36864
	ds_write_b64 v227, v[148:149] offset:49152
	s_waitcnt lgkmcnt(9)
	v_mfma_f32_16x16x32_bf16 v[64:67], v[176:179], v[104:107], v[64:67]
	v_add_f32_e32 v220, v220, v88
	v_mfma_f32_16x16x32_bf16 v[68:71], v[176:179], v[120:123], v[68:71]
	v_add_f32_e32 v221, v221, v92
	ds_read_b128 v[172:175], v209 offset:26624
	ds_write_b64 v228, v[150:151] offset:49152
	s_waitcnt lgkmcnt(10)
	v_mfma_f32_16x16x32_bf16 v[16:19], v[180:183], v[216:219], v[16:19]
	v_add_f32_e32 v220, v220, v89
	v_mfma_f32_16x16x32_bf16 v[20:23], v[180:183], v[238:241], v[20:23]
	v_add_f32_e32 v221, v221, v93
	ds_read_b128 v[176:179], v203 offset:36864
	ds_write_b64 v229, v[144:145] offset:49152
	s_waitcnt lgkmcnt(11)
	v_mfma_f32_16x16x32_bf16 v[68:71], v[230:233], v[124:127], v[68:71]
	v_cvt_pk_bf16_f32 v244, v88, v89
	v_mfma_f32_16x16x32_bf16 v[64:67], v[230:233], v[108:111], v[64:67]
	v_cvt_pk_bf16_f32 v245, v90, v91
	ds_read_b128 v[180:183], v209 offset:28672
	ds_write_b64 v184, v[146:147] offset:49152
	s_waitcnt lgkmcnt(12)
	v_mfma_f32_16x16x32_bf16 v[28:31], v[234:237], v[238:241], v[28:31]
	v_cvt_pk_bf16_f32 v206, v92, v93
	v_mfma_f32_16x16x32_bf16 v[24:27], v[234:237], v[216:219], v[24:27]
	v_cvt_pk_bf16_f32 v207, v94, v95
	ds_read_b128 v[230:233], v246 offset:36864
	global_load_dwordx4 v[148:151], v198, s[8:9]
	s_waitcnt lgkmcnt(12)
	v_mfma_f32_16x16x32_bf16 v[72:75], v[160:163], v[96:99], 0
	v_add_f32_e32 v220, v220, v90
	v_add_f32_e32 v221, v221, v94
	v_mfma_f32_16x16x32_bf16 v[76:79], v[160:163], v[112:115], 0
	v_add_f32_e32 v220, v220, v91
	v_add_f32_e32 v221, v221, v95
	ds_read_b128 v[234:237], v209 offset:30720
	global_load_dwordx4 v[144:147], v199, s[8:9]
	s_waitcnt lgkmcnt(11)
	v_mfma_f32_16x16x32_bf16 v[32:35], v[164:167], v[216:219], v[32:35]
	v_add_f32_e32 v194, v194, v220
	v_add_f32_e32 v195, v195, v221
	v_mfma_f32_16x16x32_bf16 v[36:39], v[164:167], v[238:241], v[36:39]
	v_exp_f32_e32 v64, v64
	v_exp_f32_e32 v68, v68
	ds_read_b128 v[160:163], v201 offset:40960
	global_load_dwordx4 v[136:139], v196, s[6:7]
	s_waitcnt lgkmcnt(10)
	v_mfma_f32_16x16x32_bf16 v[76:79], v[168:171], v[116:119], v[76:79]
	v_exp_f32_e32 v65, v65
	v_mfma_f32_16x16x32_bf16 v[72:75], v[168:171], v[100:103], v[72:75]
	v_exp_f32_e32 v69, v69
	ds_read_b128 v[164:167], v210 offset:16384
	global_load_dwordx4 v[140:143], v197, s[6:7]
	s_waitcnt lgkmcnt(9)
	v_mfma_f32_16x16x32_bf16 v[44:47], v[172:175], v[238:241], v[44:47]
	v_exp_f32_e32 v66, v66
	v_mfma_f32_16x16x32_bf16 v[40:43], v[172:175], v[216:219], v[40:43]
	v_exp_f32_e32 v70, v70
	ds_read_b128 v[168:171], v202 offset:40960
	s_waitcnt lgkmcnt(8)
	v_mfma_f32_16x16x32_bf16 v[72:75], v[176:179], v[104:107], v[72:75]
	v_exp_f32_e32 v67, v67
	v_mfma_f32_16x16x32_bf16 v[76:79], v[176:179], v[120:123], v[76:79]
	v_exp_f32_e32 v71, v71
	ds_read_b128 v[172:175], v210 offset:18432
	s_waitcnt lgkmcnt(7)
	v_mfma_f32_16x16x32_bf16 v[48:51], v[180:183], v[216:219], v[48:51]
	v_add_f32_e32 v220, v64, v65
	v_mfma_f32_16x16x32_bf16 v[52:55], v[180:183], v[238:241], v[52:55]
	v_add_f32_e32 v221, v68, v69
	ds_read_b128 v[176:179], v203 offset:40960
	s_waitcnt lgkmcnt(6)
	v_mfma_f32_16x16x32_bf16 v[76:79], v[230:233], v[124:127], v[76:79]
	v_add_f32_e32 v220, v220, v66
	v_mfma_f32_16x16x32_bf16 v[72:75], v[230:233], v[108:111], v[72:75]
	v_add_f32_e32 v221, v221, v70
	ds_read_b128 v[180:183], v210 offset:20480
	s_waitcnt lgkmcnt(6)
	v_mfma_f32_16x16x32_bf16 v[60:63], v[234:237], v[238:241], v[60:63]
	v_add_f32_e32 v220, v220, v67
	v_mfma_f32_16x16x32_bf16 v[56:59], v[234:237], v[216:219], v[56:59]
	v_add_f32_e32 v221, v221, v71
	ds_read_b128 v[230:233], v246 offset:40960
	s_waitcnt lgkmcnt(6)
	v_mfma_f32_16x16x32_bf16 v[80:83], v[160:163], v[96:99], 0
	v_exp_f32_e32 v72, v72
	v_exp_f32_e32 v76, v76
	v_mfma_f32_16x16x32_bf16 v[84:87], v[160:163], v[112:115], 0
	v_exp_f32_e32 v73, v73
	v_exp_f32_e32 v77, v77
	ds_read_b128 v[234:237], v210 offset:22528
	s_waitcnt lgkmcnt(6)
	v_mfma_f32_16x16x32_bf16 v[0:3], v[164:167], v[242:245], v[0:3]
	v_exp_f32_e32 v74, v74
	v_exp_f32_e32 v78, v78
	v_mfma_f32_16x16x32_bf16 v[4:7], v[164:167], v[204:207], v[4:7]
	v_exp_f32_e32 v75, v75
	v_exp_f32_e32 v79, v79
	ds_read_b128 v[160:163], v201 offset:45056
	s_waitcnt lgkmcnt(6)
	v_mfma_f32_16x16x32_bf16 v[84:87], v[168:171], v[116:119], v[84:87]
	v_add_f32_e32 v220, v220, v72
	v_mfma_f32_16x16x32_bf16 v[80:83], v[168:171], v[100:103], v[80:83]
	v_add_f32_e32 v221, v221, v76
	ds_read_b128 v[164:167], v210 offset:24576
	s_waitcnt lgkmcnt(6)
	v_mfma_f32_16x16x32_bf16 v[12:15], v[172:175], v[204:207], v[12:15]
	v_add_f32_e32 v220, v220, v73
	v_mfma_f32_16x16x32_bf16 v[8:11], v[172:175], v[242:245], v[8:11]
	v_add_f32_e32 v221, v221, v77
	ds_read_b128 v[168:171], v202 offset:45056
	s_waitcnt lgkmcnt(6)
	v_mfma_f32_16x16x32_bf16 v[80:83], v[176:179], v[104:107], v[80:83]
	v_add_f32_e32 v220, v220, v74
	v_mfma_f32_16x16x32_bf16 v[84:87], v[176:179], v[120:123], v[84:87]
	v_add_f32_e32 v221, v221, v78
	ds_read_b128 v[172:175], v210 offset:26624
	s_waitcnt lgkmcnt(6)
	v_mfma_f32_16x16x32_bf16 v[16:19], v[180:183], v[242:245], v[16:19]
	v_add_f32_e32 v220, v220, v75
	v_mfma_f32_16x16x32_bf16 v[20:23], v[180:183], v[204:207], v[20:23]
	v_add_f32_e32 v221, v221, v79
	ds_read_b128 v[176:179], v203 offset:45056
	s_waitcnt lgkmcnt(6)
	v_mfma_f32_16x16x32_bf16 v[84:87], v[230:233], v[124:127], v[84:87]
	v_cvt_pk_bf16_f32 v216, v64, v65
	v_mfma_f32_16x16x32_bf16 v[80:83], v[230:233], v[108:111], v[80:83]
	v_cvt_pk_bf16_f32 v217, v66, v67
	ds_read_b128 v[180:183], v210 offset:28672
	s_waitcnt lgkmcnt(6)
	v_mfma_f32_16x16x32_bf16 v[28:31], v[234:237], v[204:207], v[28:31]
	v_cvt_pk_bf16_f32 v238, v68, v69
	v_mfma_f32_16x16x32_bf16 v[24:27], v[234:237], v[242:245], v[24:27]
	v_cvt_pk_bf16_f32 v239, v70, v71
	ds_read_b128 v[230:233], v246 offset:45056
	s_waitcnt lgkmcnt(6)
	v_mfma_f32_16x16x32_bf16 v[88:91], v[160:163], v[96:99], 0
	v_exp_f32_e32 v80, v80
	v_exp_f32_e32 v84, v84
	v_mfma_f32_16x16x32_bf16 v[92:95], v[160:163], v[112:115], 0
	v_exp_f32_e32 v81, v81
	v_exp_f32_e32 v85, v85
	ds_read_b128 v[234:237], v210 offset:30720
	s_waitcnt lgkmcnt(6)
	v_mfma_f32_16x16x32_bf16 v[32:35], v[164:167], v[242:245], v[32:35]
	v_exp_f32_e32 v82, v82
	v_exp_f32_e32 v86, v86
	v_mfma_f32_16x16x32_bf16 v[36:39], v[164:167], v[204:207], v[36:39]
	v_exp_f32_e32 v83, v83
	v_exp_f32_e32 v87, v87
	s_waitcnt lgkmcnt(5)
	v_mfma_f32_16x16x32_bf16 v[92:95], v[168:171], v[116:119], v[92:95]
	v_add_f32_e32 v220, v220, v80
	v_mfma_f32_16x16x32_bf16 v[88:91], v[168:171], v[100:103], v[88:91]
	v_add_f32_e32 v221, v221, v84
	s_waitcnt lgkmcnt(4)
	v_mfma_f32_16x16x32_bf16 v[44:47], v[172:175], v[204:207], v[44:47]
	v_add_f32_e32 v220, v220, v81
	v_mfma_f32_16x16x32_bf16 v[40:43], v[172:175], v[242:245], v[40:43]
	v_add_f32_e32 v221, v221, v85
	s_waitcnt lgkmcnt(3)
	v_mfma_f32_16x16x32_bf16 v[88:91], v[176:179], v[104:107], v[88:91]
	v_add_f32_e32 v220, v220, v82
	v_mfma_f32_16x16x32_bf16 v[92:95], v[176:179], v[120:123], v[92:95]
	v_add_f32_e32 v221, v221, v86
	s_waitcnt lgkmcnt(2)
	v_mfma_f32_16x16x32_bf16 v[48:51], v[180:183], v[242:245], v[48:51]
	v_add_f32_e32 v220, v220, v83
	v_mfma_f32_16x16x32_bf16 v[52:55], v[180:183], v[204:207], v[52:55]
	v_add_f32_e32 v221, v221, v87
	s_waitcnt lgkmcnt(1)
	v_mfma_f32_16x16x32_bf16 v[92:95], v[230:233], v[124:127], v[92:95]
	v_cvt_pk_bf16_f32 v218, v72, v73
	v_mfma_f32_16x16x32_bf16 v[88:91], v[230:233], v[108:111], v[88:91]
	v_cvt_pk_bf16_f32 v219, v74, v75
	s_waitcnt lgkmcnt(0)
	v_mfma_f32_16x16x32_bf16 v[60:63], v[234:237], v[204:207], v[60:63]
	v_cvt_pk_bf16_f32 v240, v76, v77
	v_mfma_f32_16x16x32_bf16 v[56:59], v[234:237], v[242:245], v[56:59]
	v_cvt_pk_bf16_f32 v241, v78, v79
	s_waitcnt lgkmcnt(0)
	s_barrier
	ds_read_b128 v[160:163], v201 offset:49152
	ds_read_b128 v[164:167], v209 offset:32768
	ds_read_b128 v[168:171], v202 offset:49152
	ds_read_b128 v[172:175], v209 offset:34816
	ds_read_b128 v[176:179], v203 offset:49152
	ds_read_b128 v[180:183], v209 offset:36864
	ds_read_b128 v[230:233], v246 offset:49152
	s_waitcnt lgkmcnt(6)
	v_mfma_f32_16x16x32_bf16 v[64:67], v[160:163], v[96:99], 0
	v_exp_f32_e32 v88, v88
	v_exp_f32_e32 v92, v92
	v_mfma_f32_16x16x32_bf16 v[68:71], v[160:163], v[112:115], 0
	v_cvt_pk_bf16_f32 v242, v80, v81
	v_exp_f32_e32 v89, v89
	ds_read_b128 v[234:237], v209 offset:38912
	s_add_u32 s8, s16, 0x3bc00300
	s_addc_u32 s9, s17, 0
	s_add_u32 s6, s15, 0x23a70000
	s_addc_u32 s7, s14, 0
	s_waitcnt lgkmcnt(6)
	v_mfma_f32_16x16x32_bf16 v[0:3], v[164:167], v[216:219], v[0:3]
	v_exp_f32_e32 v93, v93
	v_cvt_pk_bf16_f32 v243, v82, v83
	v_mfma_f32_16x16x32_bf16 v[4:7], v[164:167], v[238:241], v[4:7]
	v_exp_f32_e32 v90, v90
	v_exp_f32_e32 v94, v94
	ds_read_b128 v[160:163], v201 offset:53248
	s_waitcnt vmcnt(4)
	ds_write_b128 v225, v[152:155] offset:16384
	s_waitcnt lgkmcnt(7)
	v_mfma_f32_16x16x32_bf16 v[68:71], v[168:171], v[116:119], v[68:71]
	v_cvt_pk_bf16_f32 v204, v84, v85
	v_mfma_f32_16x16x32_bf16 v[64:67], v[168:171], v[100:103], v[64:67]
	v_exp_f32_e32 v91, v91
	ds_read_b128 v[164:167], v209 offset:40960
	ds_write_b128 v226, v[156:159] offset:16384
	s_waitcnt lgkmcnt(8)
	v_mfma_f32_16x16x32_bf16 v[12:15], v[172:175], v[238:241], v[12:15]
	v_exp_f32_e32 v95, v95
	v_mfma_f32_16x16x32_bf16 v[8:11], v[172:175], v[216:219], v[8:11]
	v_cvt_pk_bf16_f32 v205, v86, v87
	ds_read_b128 v[168:171], v202 offset:53248
	ds_write_b64 v227, v[132:133] offset:0
	s_waitcnt lgkmcnt(9)
	v_mfma_f32_16x16x32_bf16 v[64:67], v[176:179], v[104:107], v[64:67]
	v_add_f32_e32 v220, v220, v88
	v_mfma_f32_16x16x32_bf16 v[68:71], v[176:179], v[120:123], v[68:71]
	v_add_f32_e32 v221, v221, v92
	ds_read_b128 v[172:175], v209 offset:43008
	ds_write_b64 v228, v[134:135] offset:0
	s_waitcnt lgkmcnt(10)
	v_mfma_f32_16x16x32_bf16 v[16:19], v[180:183], v[216:219], v[16:19]
	v_add_f32_e32 v220, v220, v89
	v_mfma_f32_16x16x32_bf16 v[20:23], v[180:183], v[238:241], v[20:23]
	v_add_f32_e32 v221, v221, v93
	ds_read_b128 v[176:179], v203 offset:53248
	ds_write_b64 v229, v[128:129] offset:0
	s_waitcnt lgkmcnt(11)
	v_mfma_f32_16x16x32_bf16 v[68:71], v[230:233], v[124:127], v[68:71]
	v_cvt_pk_bf16_f32 v244, v88, v89
	v_mfma_f32_16x16x32_bf16 v[64:67], v[230:233], v[108:111], v[64:67]
	v_cvt_pk_bf16_f32 v245, v90, v91
	ds_read_b128 v[180:183], v209 offset:45056
	ds_write_b64 v184, v[130:131] offset:0
	s_waitcnt lgkmcnt(12)
	v_mfma_f32_16x16x32_bf16 v[28:31], v[234:237], v[238:241], v[28:31]
	v_cvt_pk_bf16_f32 v206, v92, v93
	v_mfma_f32_16x16x32_bf16 v[24:27], v[234:237], v[216:219], v[24:27]
	v_cvt_pk_bf16_f32 v207, v94, v95
	ds_read_b128 v[230:233], v246 offset:53248
	global_load_dwordx4 v[132:135], v198, s[8:9]
	s_waitcnt lgkmcnt(12)
	v_mfma_f32_16x16x32_bf16 v[72:75], v[160:163], v[96:99], 0
	v_add_f32_e32 v220, v220, v90
	v_add_f32_e32 v221, v221, v94
	v_mfma_f32_16x16x32_bf16 v[76:79], v[160:163], v[112:115], 0
	v_add_f32_e32 v220, v220, v91
	v_add_f32_e32 v221, v221, v95
	ds_read_b128 v[234:237], v209 offset:47104
	global_load_dwordx4 v[128:131], v199, s[8:9]
	s_waitcnt lgkmcnt(11)
	v_mfma_f32_16x16x32_bf16 v[32:35], v[164:167], v[216:219], v[32:35]
	v_add_f32_e32 v194, v194, v220
	v_add_f32_e32 v195, v195, v221
	v_mfma_f32_16x16x32_bf16 v[36:39], v[164:167], v[238:241], v[36:39]
	v_exp_f32_e32 v64, v64
	v_exp_f32_e32 v68, v68
	ds_read_b128 v[160:163], v201 offset:57344
	global_load_dwordx4 v[152:155], v196, s[6:7]
	s_waitcnt lgkmcnt(10)
	v_mfma_f32_16x16x32_bf16 v[76:79], v[168:171], v[116:119], v[76:79]
	v_exp_f32_e32 v65, v65
	v_mfma_f32_16x16x32_bf16 v[72:75], v[168:171], v[100:103], v[72:75]
	v_exp_f32_e32 v69, v69
	ds_read_b128 v[164:167], v210 offset:32768
	global_load_dwordx4 v[156:159], v197, s[6:7]
	s_waitcnt lgkmcnt(9)
	v_mfma_f32_16x16x32_bf16 v[44:47], v[172:175], v[238:241], v[44:47]
	v_exp_f32_e32 v66, v66
	v_mfma_f32_16x16x32_bf16 v[40:43], v[172:175], v[216:219], v[40:43]
	v_exp_f32_e32 v70, v70
	ds_read_b128 v[168:171], v202 offset:57344
	s_waitcnt lgkmcnt(8)
	v_mfma_f32_16x16x32_bf16 v[72:75], v[176:179], v[104:107], v[72:75]
	v_exp_f32_e32 v67, v67
	v_mfma_f32_16x16x32_bf16 v[76:79], v[176:179], v[120:123], v[76:79]
	v_exp_f32_e32 v71, v71
	ds_read_b128 v[172:175], v210 offset:34816
	s_waitcnt lgkmcnt(7)
	v_mfma_f32_16x16x32_bf16 v[48:51], v[180:183], v[216:219], v[48:51]
	v_add_f32_e32 v220, v64, v65
	v_mfma_f32_16x16x32_bf16 v[52:55], v[180:183], v[238:241], v[52:55]
	v_add_f32_e32 v221, v68, v69
	ds_read_b128 v[176:179], v203 offset:57344
	s_waitcnt lgkmcnt(6)
	v_mfma_f32_16x16x32_bf16 v[76:79], v[230:233], v[124:127], v[76:79]
	v_add_f32_e32 v220, v220, v66
	v_mfma_f32_16x16x32_bf16 v[72:75], v[230:233], v[108:111], v[72:75]
	v_add_f32_e32 v221, v221, v70
	ds_read_b128 v[180:183], v210 offset:36864
	s_waitcnt lgkmcnt(6)
	v_mfma_f32_16x16x32_bf16 v[60:63], v[234:237], v[238:241], v[60:63]
	v_add_f32_e32 v220, v220, v67
	v_mfma_f32_16x16x32_bf16 v[56:59], v[234:237], v[216:219], v[56:59]
	v_add_f32_e32 v221, v221, v71
	ds_read_b128 v[230:233], v246 offset:57344
	s_waitcnt lgkmcnt(6)
	v_mfma_f32_16x16x32_bf16 v[80:83], v[160:163], v[96:99], 0
	v_exp_f32_e32 v72, v72
	v_exp_f32_e32 v76, v76
	v_mfma_f32_16x16x32_bf16 v[84:87], v[160:163], v[112:115], 0
	v_exp_f32_e32 v73, v73
	v_exp_f32_e32 v77, v77
	ds_read_b128 v[234:237], v210 offset:38912
	s_waitcnt lgkmcnt(6)
	v_mfma_f32_16x16x32_bf16 v[0:3], v[164:167], v[242:245], v[0:3]
	v_exp_f32_e32 v74, v74
	v_exp_f32_e32 v78, v78
	v_mfma_f32_16x16x32_bf16 v[4:7], v[164:167], v[204:207], v[4:7]
	v_exp_f32_e32 v75, v75
	v_exp_f32_e32 v79, v79
	ds_read_b128 v[160:163], v201 offset:61440
	s_waitcnt lgkmcnt(6)
	v_mfma_f32_16x16x32_bf16 v[84:87], v[168:171], v[116:119], v[84:87]
	v_add_f32_e32 v220, v220, v72
	v_mfma_f32_16x16x32_bf16 v[80:83], v[168:171], v[100:103], v[80:83]
	v_add_f32_e32 v221, v221, v76
	ds_read_b128 v[164:167], v210 offset:40960
	s_waitcnt lgkmcnt(6)
	v_mfma_f32_16x16x32_bf16 v[12:15], v[172:175], v[204:207], v[12:15]
	v_add_f32_e32 v220, v220, v73
	v_mfma_f32_16x16x32_bf16 v[8:11], v[172:175], v[242:245], v[8:11]
	v_add_f32_e32 v221, v221, v77
	ds_read_b128 v[168:171], v202 offset:61440
	s_waitcnt lgkmcnt(6)
	v_mfma_f32_16x16x32_bf16 v[80:83], v[176:179], v[104:107], v[80:83]
	v_add_f32_e32 v220, v220, v74
	v_mfma_f32_16x16x32_bf16 v[84:87], v[176:179], v[120:123], v[84:87]
	v_add_f32_e32 v221, v221, v78
	ds_read_b128 v[172:175], v210 offset:43008
	s_waitcnt lgkmcnt(6)
	v_mfma_f32_16x16x32_bf16 v[16:19], v[180:183], v[242:245], v[16:19]
	v_add_f32_e32 v220, v220, v75
	v_mfma_f32_16x16x32_bf16 v[20:23], v[180:183], v[204:207], v[20:23]
	v_add_f32_e32 v221, v221, v79
	ds_read_b128 v[176:179], v203 offset:61440
	s_waitcnt lgkmcnt(6)
	v_mfma_f32_16x16x32_bf16 v[84:87], v[230:233], v[124:127], v[84:87]
	v_cvt_pk_bf16_f32 v216, v64, v65
	v_mfma_f32_16x16x32_bf16 v[80:83], v[230:233], v[108:111], v[80:83]
	v_cvt_pk_bf16_f32 v217, v66, v67
	ds_read_b128 v[180:183], v210 offset:45056
	s_waitcnt lgkmcnt(6)
	v_mfma_f32_16x16x32_bf16 v[28:31], v[234:237], v[204:207], v[28:31]
	v_cvt_pk_bf16_f32 v238, v68, v69
	v_mfma_f32_16x16x32_bf16 v[24:27], v[234:237], v[242:245], v[24:27]
	v_cvt_pk_bf16_f32 v239, v70, v71
	ds_read_b128 v[230:233], v246 offset:61440
	s_waitcnt lgkmcnt(6)
	v_mfma_f32_16x16x32_bf16 v[88:91], v[160:163], v[96:99], 0
	v_exp_f32_e32 v80, v80
	v_exp_f32_e32 v84, v84
	v_mfma_f32_16x16x32_bf16 v[92:95], v[160:163], v[112:115], 0
	v_exp_f32_e32 v81, v81
	v_exp_f32_e32 v85, v85
	ds_read_b128 v[234:237], v210 offset:47104
	s_waitcnt lgkmcnt(6)
	v_mfma_f32_16x16x32_bf16 v[32:35], v[164:167], v[242:245], v[32:35]
	v_exp_f32_e32 v82, v82
	v_exp_f32_e32 v86, v86
	v_mfma_f32_16x16x32_bf16 v[36:39], v[164:167], v[204:207], v[36:39]
	v_exp_f32_e32 v83, v83
	v_exp_f32_e32 v87, v87
	ds_read_b128 v[160:163], v201 offset:0
	s_waitcnt lgkmcnt(6)
	v_mfma_f32_16x16x32_bf16 v[92:95], v[168:171], v[116:119], v[92:95]
	v_add_f32_e32 v220, v220, v80
	v_mfma_f32_16x16x32_bf16 v[88:91], v[168:171], v[100:103], v[88:91]
	v_add_f32_e32 v221, v221, v84
	ds_read_b128 v[164:167], v209 offset:49152
	s_waitcnt lgkmcnt(6)
	v_mfma_f32_16x16x32_bf16 v[44:47], v[172:175], v[204:207], v[44:47]
	v_add_f32_e32 v220, v220, v81
	v_mfma_f32_16x16x32_bf16 v[40:43], v[172:175], v[242:245], v[40:43]
	v_add_f32_e32 v221, v221, v85
	ds_read_b128 v[168:171], v202 offset:0
	s_waitcnt lgkmcnt(6)
	v_mfma_f32_16x16x32_bf16 v[88:91], v[176:179], v[104:107], v[88:91]
	v_add_f32_e32 v220, v220, v82
	v_mfma_f32_16x16x32_bf16 v[92:95], v[176:179], v[120:123], v[92:95]
	v_add_f32_e32 v221, v221, v86
	ds_read_b128 v[172:175], v209 offset:51200
	s_waitcnt lgkmcnt(6)
	v_mfma_f32_16x16x32_bf16 v[48:51], v[180:183], v[242:245], v[48:51]
	v_add_f32_e32 v220, v220, v83
	v_mfma_f32_16x16x32_bf16 v[52:55], v[180:183], v[204:207], v[52:55]
	v_add_f32_e32 v221, v221, v87
	ds_read_b128 v[176:179], v203 offset:0
	s_waitcnt lgkmcnt(6)
	v_mfma_f32_16x16x32_bf16 v[92:95], v[230:233], v[124:127], v[92:95]
	v_cvt_pk_bf16_f32 v218, v72, v73
	v_mfma_f32_16x16x32_bf16 v[88:91], v[230:233], v[108:111], v[88:91]
	v_cvt_pk_bf16_f32 v219, v74, v75
	ds_read_b128 v[180:183], v209 offset:53248
	s_waitcnt lgkmcnt(6)
	v_mfma_f32_16x16x32_bf16 v[60:63], v[234:237], v[204:207], v[60:63]
	v_cvt_pk_bf16_f32 v240, v76, v77
	v_mfma_f32_16x16x32_bf16 v[56:59], v[234:237], v[242:245], v[56:59]
	v_cvt_pk_bf16_f32 v241, v78, v79
	ds_read_b128 v[230:233], v246 offset:0
	s_waitcnt lgkmcnt(6)
	v_mfma_f32_16x16x32_bf16 v[64:67], v[160:163], v[96:99], 0
	v_exp_f32_e32 v88, v88
	v_exp_f32_e32 v92, v92
	v_mfma_f32_16x16x32_bf16 v[68:71], v[160:163], v[112:115], 0
	v_cvt_pk_bf16_f32 v242, v80, v81
	v_exp_f32_e32 v89, v89
	ds_read_b128 v[234:237], v209 offset:55296
	s_add_u32 s8, s16, 0x3bc00380
	s_addc_u32 s9, s17, 0
	s_add_u32 s6, s15, 0x23a80000
	s_addc_u32 s7, s14, 0
	s_waitcnt lgkmcnt(6)
	v_mfma_f32_16x16x32_bf16 v[0:3], v[164:167], v[216:219], v[0:3]
	v_exp_f32_e32 v93, v93
	v_cvt_pk_bf16_f32 v243, v82, v83
	v_mfma_f32_16x16x32_bf16 v[4:7], v[164:167], v[238:241], v[4:7]
	v_exp_f32_e32 v90, v90
	v_exp_f32_e32 v94, v94
	ds_read_b128 v[160:163], v201 offset:4096
	s_waitcnt vmcnt(4)
	ds_write_b128 v225, v[136:139] offset:32768
	s_waitcnt lgkmcnt(7)
	v_mfma_f32_16x16x32_bf16 v[68:71], v[168:171], v[116:119], v[68:71]
	v_cvt_pk_bf16_f32 v204, v84, v85
	v_mfma_f32_16x16x32_bf16 v[64:67], v[168:171], v[100:103], v[64:67]
	v_exp_f32_e32 v91, v91
	ds_read_b128 v[164:167], v209 offset:57344
	ds_write_b128 v226, v[140:143] offset:32768
	s_waitcnt lgkmcnt(8)
	v_mfma_f32_16x16x32_bf16 v[12:15], v[172:175], v[238:241], v[12:15]
	v_exp_f32_e32 v95, v95
	v_mfma_f32_16x16x32_bf16 v[8:11], v[172:175], v[216:219], v[8:11]
	v_cvt_pk_bf16_f32 v205, v86, v87
	ds_read_b128 v[168:171], v202 offset:4096
	ds_write_b64 v227, v[148:149] offset:16384
	s_waitcnt lgkmcnt(9)
	v_mfma_f32_16x16x32_bf16 v[64:67], v[176:179], v[104:107], v[64:67]
	v_add_f32_e32 v220, v220, v88
	v_mfma_f32_16x16x32_bf16 v[68:71], v[176:179], v[120:123], v[68:71]
	v_add_f32_e32 v221, v221, v92
	ds_read_b128 v[172:175], v209 offset:59392
	ds_write_b64 v228, v[150:151] offset:16384
	s_waitcnt lgkmcnt(10)
	v_mfma_f32_16x16x32_bf16 v[16:19], v[180:183], v[216:219], v[16:19]
	v_add_f32_e32 v220, v220, v89
	v_mfma_f32_16x16x32_bf16 v[20:23], v[180:183], v[238:241], v[20:23]
	v_add_f32_e32 v221, v221, v93
	ds_read_b128 v[176:179], v203 offset:4096
	ds_write_b64 v229, v[144:145] offset:16384
	s_waitcnt lgkmcnt(11)
	v_mfma_f32_16x16x32_bf16 v[68:71], v[230:233], v[124:127], v[68:71]
	v_cvt_pk_bf16_f32 v244, v88, v89
	v_mfma_f32_16x16x32_bf16 v[64:67], v[230:233], v[108:111], v[64:67]
	v_cvt_pk_bf16_f32 v245, v90, v91
	ds_read_b128 v[180:183], v209 offset:61440
	ds_write_b64 v184, v[146:147] offset:16384
	s_waitcnt lgkmcnt(12)
	v_mfma_f32_16x16x32_bf16 v[28:31], v[234:237], v[238:241], v[28:31]
	v_cvt_pk_bf16_f32 v206, v92, v93
	v_mfma_f32_16x16x32_bf16 v[24:27], v[234:237], v[216:219], v[24:27]
	v_cvt_pk_bf16_f32 v207, v94, v95
	ds_read_b128 v[230:233], v246 offset:4096
	global_load_dwordx4 v[148:151], v198, s[8:9]
	s_waitcnt lgkmcnt(12)
	v_mfma_f32_16x16x32_bf16 v[72:75], v[160:163], v[96:99], 0
	v_add_f32_e32 v220, v220, v90
	v_add_f32_e32 v221, v221, v94
	v_mfma_f32_16x16x32_bf16 v[76:79], v[160:163], v[112:115], 0
	v_add_f32_e32 v220, v220, v91
	v_add_f32_e32 v221, v221, v95
	ds_read_b128 v[234:237], v209 offset:63488
	global_load_dwordx4 v[144:147], v199, s[8:9]
	s_waitcnt lgkmcnt(11)
	v_mfma_f32_16x16x32_bf16 v[32:35], v[164:167], v[216:219], v[32:35]
	v_add_f32_e32 v194, v194, v220
	v_add_f32_e32 v195, v195, v221
	v_mfma_f32_16x16x32_bf16 v[36:39], v[164:167], v[238:241], v[36:39]
	v_exp_f32_e32 v64, v64
	v_exp_f32_e32 v68, v68
	ds_read_b128 v[160:163], v201 offset:8192
	global_load_dwordx4 v[136:139], v196, s[6:7]
	s_waitcnt lgkmcnt(10)
	v_mfma_f32_16x16x32_bf16 v[76:79], v[168:171], v[116:119], v[76:79]
	v_exp_f32_e32 v65, v65
	v_mfma_f32_16x16x32_bf16 v[72:75], v[168:171], v[100:103], v[72:75]
	v_exp_f32_e32 v69, v69
	ds_read_b128 v[164:167], v210 offset:49152
	global_load_dwordx4 v[140:143], v197, s[6:7]
	s_waitcnt lgkmcnt(9)
	v_mfma_f32_16x16x32_bf16 v[44:47], v[172:175], v[238:241], v[44:47]
	v_exp_f32_e32 v66, v66
	v_mfma_f32_16x16x32_bf16 v[40:43], v[172:175], v[216:219], v[40:43]
	v_exp_f32_e32 v70, v70
	ds_read_b128 v[168:171], v202 offset:8192
	s_waitcnt lgkmcnt(8)
	v_mfma_f32_16x16x32_bf16 v[72:75], v[176:179], v[104:107], v[72:75]
	v_exp_f32_e32 v67, v67
	v_mfma_f32_16x16x32_bf16 v[76:79], v[176:179], v[120:123], v[76:79]
	v_exp_f32_e32 v71, v71
	ds_read_b128 v[172:175], v210 offset:51200
	s_waitcnt lgkmcnt(7)
	v_mfma_f32_16x16x32_bf16 v[48:51], v[180:183], v[216:219], v[48:51]
	v_add_f32_e32 v220, v64, v65
	v_mfma_f32_16x16x32_bf16 v[52:55], v[180:183], v[238:241], v[52:55]
	v_add_f32_e32 v221, v68, v69
	ds_read_b128 v[176:179], v203 offset:8192
	s_waitcnt lgkmcnt(6)
	v_mfma_f32_16x16x32_bf16 v[76:79], v[230:233], v[124:127], v[76:79]
	v_add_f32_e32 v220, v220, v66
	v_mfma_f32_16x16x32_bf16 v[72:75], v[230:233], v[108:111], v[72:75]
	v_add_f32_e32 v221, v221, v70
	ds_read_b128 v[180:183], v210 offset:53248
	s_waitcnt lgkmcnt(6)
	v_mfma_f32_16x16x32_bf16 v[60:63], v[234:237], v[238:241], v[60:63]
	v_add_f32_e32 v220, v220, v67
	v_mfma_f32_16x16x32_bf16 v[56:59], v[234:237], v[216:219], v[56:59]
	v_add_f32_e32 v221, v221, v71
	ds_read_b128 v[230:233], v246 offset:8192
	s_waitcnt lgkmcnt(6)
	v_mfma_f32_16x16x32_bf16 v[80:83], v[160:163], v[96:99], 0
	v_exp_f32_e32 v72, v72
	v_exp_f32_e32 v76, v76
	v_mfma_f32_16x16x32_bf16 v[84:87], v[160:163], v[112:115], 0
	v_exp_f32_e32 v73, v73
	v_exp_f32_e32 v77, v77
	ds_read_b128 v[234:237], v210 offset:55296
	s_waitcnt lgkmcnt(6)
	v_mfma_f32_16x16x32_bf16 v[0:3], v[164:167], v[242:245], v[0:3]
	v_exp_f32_e32 v74, v74
	v_exp_f32_e32 v78, v78
	v_mfma_f32_16x16x32_bf16 v[4:7], v[164:167], v[204:207], v[4:7]
	v_exp_f32_e32 v75, v75
	v_exp_f32_e32 v79, v79
	ds_read_b128 v[160:163], v201 offset:12288
	s_waitcnt lgkmcnt(6)
	v_mfma_f32_16x16x32_bf16 v[84:87], v[168:171], v[116:119], v[84:87]
	v_add_f32_e32 v220, v220, v72
	v_mfma_f32_16x16x32_bf16 v[80:83], v[168:171], v[100:103], v[80:83]
	v_add_f32_e32 v221, v221, v76
	ds_read_b128 v[164:167], v210 offset:57344
	s_waitcnt lgkmcnt(6)
	v_mfma_f32_16x16x32_bf16 v[12:15], v[172:175], v[204:207], v[12:15]
	v_add_f32_e32 v220, v220, v73
	v_mfma_f32_16x16x32_bf16 v[8:11], v[172:175], v[242:245], v[8:11]
	v_add_f32_e32 v221, v221, v77
	ds_read_b128 v[168:171], v202 offset:12288
	s_waitcnt lgkmcnt(6)
	v_mfma_f32_16x16x32_bf16 v[80:83], v[176:179], v[104:107], v[80:83]
	v_add_f32_e32 v220, v220, v74
	v_mfma_f32_16x16x32_bf16 v[84:87], v[176:179], v[120:123], v[84:87]
	v_add_f32_e32 v221, v221, v78
	ds_read_b128 v[172:175], v210 offset:59392
	s_add_u32 s10, s10, 0x200
	s_addc_u32 s11, s11, 0
	s_add_u32 s12, s12, 0x40000
	s_addc_u32 s13, s13, 0
	s_add_i32 s4, s4, 4
	s_cmpk_lt_u32 s4, 0x104
	s_cselect_b64 s[6:7], -1, 0
	s_and_b64 s[6:7], s[0:1], s[6:7]
	s_and_b64 vcc, exec, s[6:7]
	s_waitcnt lgkmcnt(6)
	v_mfma_f32_16x16x32_bf16 v[16:19], v[180:183], v[242:245], v[16:19]
	v_add_f32_e32 v220, v220, v75
	v_mfma_f32_16x16x32_bf16 v[20:23], v[180:183], v[204:207], v[20:23]
	v_add_f32_e32 v221, v221, v79
	ds_read_b128 v[176:179], v203 offset:12288
	s_waitcnt lgkmcnt(6)
	v_mfma_f32_16x16x32_bf16 v[84:87], v[230:233], v[124:127], v[84:87]
	v_cvt_pk_bf16_f32 v216, v64, v65
	v_mfma_f32_16x16x32_bf16 v[80:83], v[230:233], v[108:111], v[80:83]
	v_cvt_pk_bf16_f32 v217, v66, v67
	ds_read_b128 v[180:183], v210 offset:61440
	s_waitcnt lgkmcnt(6)
	v_mfma_f32_16x16x32_bf16 v[28:31], v[234:237], v[204:207], v[28:31]
	v_cvt_pk_bf16_f32 v238, v68, v69
	v_mfma_f32_16x16x32_bf16 v[24:27], v[234:237], v[242:245], v[24:27]
	v_cvt_pk_bf16_f32 v239, v70, v71
	ds_read_b128 v[230:233], v246 offset:12288
	s_waitcnt lgkmcnt(6)
	v_mfma_f32_16x16x32_bf16 v[88:91], v[160:163], v[96:99], 0
	v_exp_f32_e32 v80, v80
	v_exp_f32_e32 v84, v84
	v_mfma_f32_16x16x32_bf16 v[92:95], v[160:163], v[112:115], 0
	v_exp_f32_e32 v81, v81
	v_exp_f32_e32 v85, v85
	ds_read_b128 v[234:237], v210 offset:63488
	s_waitcnt lgkmcnt(6)
	v_mfma_f32_16x16x32_bf16 v[32:35], v[164:167], v[242:245], v[32:35]
	v_exp_f32_e32 v82, v82
	v_exp_f32_e32 v86, v86
	v_mfma_f32_16x16x32_bf16 v[36:39], v[164:167], v[204:207], v[36:39]
	v_exp_f32_e32 v83, v83
	v_exp_f32_e32 v87, v87
	s_waitcnt lgkmcnt(5)
	v_mfma_f32_16x16x32_bf16 v[92:95], v[168:171], v[116:119], v[92:95]
	v_add_f32_e32 v220, v220, v80
	v_mfma_f32_16x16x32_bf16 v[88:91], v[168:171], v[100:103], v[88:91]
	v_add_f32_e32 v221, v221, v84
	s_waitcnt lgkmcnt(4)
	v_mfma_f32_16x16x32_bf16 v[44:47], v[172:175], v[204:207], v[44:47]
	v_add_f32_e32 v220, v220, v81
	v_mfma_f32_16x16x32_bf16 v[40:43], v[172:175], v[242:245], v[40:43]
	v_add_f32_e32 v221, v221, v85
	s_waitcnt lgkmcnt(3)
	v_mfma_f32_16x16x32_bf16 v[88:91], v[176:179], v[104:107], v[88:91]
	v_add_f32_e32 v220, v220, v82
	v_mfma_f32_16x16x32_bf16 v[92:95], v[176:179], v[120:123], v[92:95]
	v_add_f32_e32 v221, v221, v86
	s_waitcnt lgkmcnt(2)
	v_mfma_f32_16x16x32_bf16 v[48:51], v[180:183], v[242:245], v[48:51]
	v_add_f32_e32 v220, v220, v83
	v_mfma_f32_16x16x32_bf16 v[52:55], v[180:183], v[204:207], v[52:55]
	v_add_f32_e32 v221, v221, v87
	s_waitcnt lgkmcnt(1)
	v_mfma_f32_16x16x32_bf16 v[92:95], v[230:233], v[124:127], v[92:95]
	v_cvt_pk_bf16_f32 v218, v72, v73
	v_mfma_f32_16x16x32_bf16 v[88:91], v[230:233], v[108:111], v[88:91]
	v_cvt_pk_bf16_f32 v219, v74, v75
	s_waitcnt lgkmcnt(0)
	v_mfma_f32_16x16x32_bf16 v[60:63], v[234:237], v[204:207], v[60:63]
	v_cvt_pk_bf16_f32 v240, v76, v77
	v_mfma_f32_16x16x32_bf16 v[56:59], v[234:237], v[242:245], v[56:59]
	v_cvt_pk_bf16_f32 v241, v78, v79
	s_cbranch_vccnz .LBB0_734
	s_setprio 0
	s_waitcnt vmcnt(0)
	s_nop 7
	s_nop 7
	ds_swizzle_b32 v64, v194 offset:swizzle(SWAP,16)
	s_waitcnt lgkmcnt(0)
	v_add_f32_e32 v194, v194, v64
	v_mov_b32_e32 v65, v194
	s_nop 1
	v_permlane32_swap_b32_e32 v194, v65
	v_add_f32_e32 v194, v194, v65
	s_nop 0
	v_rcp_f32_e32 v66, v194
	ds_swizzle_b32 v64, v195 offset:swizzle(SWAP,16)
	s_waitcnt lgkmcnt(0)
	v_add_f32_e32 v195, v195, v64
	v_mov_b32_e32 v65, v195
	s_nop 1
	v_permlane32_swap_b32_e32 v195, v65
	v_add_f32_e32 v195, v195, v65
	s_nop 0
	v_rcp_f32_e32 v67, v195
	v_readlane_b32 s100, v250, 8
	v_mbcnt_lo_u32_b32 v68, -1, 0
	v_mbcnt_hi_u32_b32 v68, -1, v68
	v_and_b32_e32 v69, 15, v68
	v_lshrrev_b32_e32 v70, 4, v68
	s_lshr_b32 s101, s100, 1
	v_add_u32_e32 v69, s101, v69
	v_lshlrev_b32_e32 v69, 12, v69
	v_and_b32_e32 v71, 1, v70
	v_lshlrev_b32_e32 v71, 5, v71
	v_and_b32_e32 v70, 2, v70
	v_lshl_add_u32 v71, v70, 3, v71
	v_add_u32_e32 v70, v69, v71
	v_add_u32_e32 v71, 0x10000, v70
	v_mul_f32_e32 v0, v0, v66
	v_mul_f32_e32 v1, v1, v66
	v_mul_f32_e32 v2, v2, v66
	v_mul_f32_e32 v3, v3, v66
	v_mul_f32_e32 v8, v8, v66
	v_mul_f32_e32 v9, v9, v66
	v_mul_f32_e32 v10, v10, v66
	v_mul_f32_e32 v11, v11, v66
	v_cvt_pk_bf16_f32 v72, v0, v1
	v_cvt_pk_bf16_f32 v73, v2, v3
	v_cvt_pk_bf16_f32 v74, v8, v9
	v_cvt_pk_bf16_f32 v75, v10, v11
	s_nop 1
	v_permlane16_swap_b32_e32 v72, v74
	v_permlane16_swap_b32_e32 v73, v75
	s_nop 1
	global_store_dwordx4 v70, v[72:75], s[58:59] offset:0
	v_mul_f32_e32 v16, v16, v66
	v_mul_f32_e32 v17, v17, v66
	v_mul_f32_e32 v18, v18, v66
	v_mul_f32_e32 v19, v19, v66
	v_mul_f32_e32 v24, v24, v66
	v_mul_f32_e32 v25, v25, v66
	v_mul_f32_e32 v26, v26, v66
	v_mul_f32_e32 v27, v27, v66
	v_cvt_pk_bf16_f32 v76, v16, v17
	v_cvt_pk_bf16_f32 v77, v18, v19
	v_cvt_pk_bf16_f32 v78, v24, v25
	v_cvt_pk_bf16_f32 v79, v26, v27
	s_nop 1
	v_permlane16_swap_b32_e32 v76, v78
	v_permlane16_swap_b32_e32 v77, v79
	s_nop 1
	global_store_dwordx4 v70, v[76:79], s[58:59] offset:64
	v_mul_f32_e32 v32, v32, v66
	v_mul_f32_e32 v33, v33, v66
	v_mul_f32_e32 v34, v34, v66
	v_mul_f32_e32 v35, v35, v66
	v_mul_f32_e32 v40, v40, v66
	v_mul_f32_e32 v41, v41, v66
	v_mul_f32_e32 v42, v42, v66
	v_mul_f32_e32 v43, v43, v66
	v_cvt_pk_bf16_f32 v80, v32, v33
	v_cvt_pk_bf16_f32 v81, v34, v35
	v_cvt_pk_bf16_f32 v82, v40, v41
	v_cvt_pk_bf16_f32 v83, v42, v43
	s_nop 1
	v_permlane16_swap_b32_e32 v80, v82
	v_permlane16_swap_b32_e32 v81, v83
	s_nop 1
	global_store_dwordx4 v70, v[80:83], s[58:59] offset:128
	v_mul_f32_e32 v48, v48, v66
	v_mul_f32_e32 v49, v49, v66
	v_mul_f32_e32 v50, v50, v66
	v_mul_f32_e32 v51, v51, v66
	v_mul_f32_e32 v56, v56, v66
	v_mul_f32_e32 v57, v57, v66
	v_mul_f32_e32 v58, v58, v66
	v_mul_f32_e32 v59, v59, v66
	v_cvt_pk_bf16_f32 v84, v48, v49
	v_cvt_pk_bf16_f32 v85, v50, v51
	v_cvt_pk_bf16_f32 v86, v56, v57
	v_cvt_pk_bf16_f32 v87, v58, v59
	s_nop 1
	v_permlane16_swap_b32_e32 v84, v86
	v_permlane16_swap_b32_e32 v85, v87
	s_nop 1
	global_store_dwordx4 v70, v[84:87], s[58:59] offset:192
	v_mul_f32_e32 v4, v4, v67
	v_mul_f32_e32 v5, v5, v67
	v_mul_f32_e32 v6, v6, v67
	v_mul_f32_e32 v7, v7, v67
	v_mul_f32_e32 v12, v12, v67
	v_mul_f32_e32 v13, v13, v67
	v_mul_f32_e32 v14, v14, v67
	v_mul_f32_e32 v15, v15, v67
	v_cvt_pk_bf16_f32 v88, v4, v5
	v_cvt_pk_bf16_f32 v89, v6, v7
	v_cvt_pk_bf16_f32 v90, v12, v13
	v_cvt_pk_bf16_f32 v91, v14, v15
	s_nop 1
	v_permlane16_swap_b32_e32 v88, v90
	v_permlane16_swap_b32_e32 v89, v91
	s_nop 1
	global_store_dwordx4 v71, v[88:91], s[58:59] offset:0
	v_mul_f32_e32 v20, v20, v67
	v_mul_f32_e32 v21, v21, v67
	v_mul_f32_e32 v22, v22, v67
	v_mul_f32_e32 v23, v23, v67
	v_mul_f32_e32 v28, v28, v67
	v_mul_f32_e32 v29, v29, v67
	v_mul_f32_e32 v30, v30, v67
	v_mul_f32_e32 v31, v31, v67
	v_cvt_pk_bf16_f32 v92, v20, v21
	v_cvt_pk_bf16_f32 v93, v22, v23
	v_cvt_pk_bf16_f32 v94, v28, v29
	v_cvt_pk_bf16_f32 v95, v30, v31
	s_nop 1
	v_permlane16_swap_b32_e32 v92, v94
	v_permlane16_swap_b32_e32 v93, v95
	s_nop 1
	global_store_dwordx4 v71, v[92:95], s[58:59] offset:64
	v_mul_f32_e32 v36, v36, v67
	v_mul_f32_e32 v37, v37, v67
	v_mul_f32_e32 v38, v38, v67
	v_mul_f32_e32 v39, v39, v67
	v_mul_f32_e32 v44, v44, v67
	v_mul_f32_e32 v45, v45, v67
	v_mul_f32_e32 v46, v46, v67
	v_mul_f32_e32 v47, v47, v67
	v_cvt_pk_bf16_f32 v72, v36, v37
	v_cvt_pk_bf16_f32 v73, v38, v39
	v_cvt_pk_bf16_f32 v74, v44, v45
	v_cvt_pk_bf16_f32 v75, v46, v47
	s_nop 1
	v_permlane16_swap_b32_e32 v72, v74
	v_permlane16_swap_b32_e32 v73, v75
	s_nop 1
	global_store_dwordx4 v71, v[72:75], s[58:59] offset:128
	v_mul_f32_e32 v52, v52, v67
	v_mul_f32_e32 v53, v53, v67
	v_mul_f32_e32 v54, v54, v67
	v_mul_f32_e32 v55, v55, v67
	v_mul_f32_e32 v60, v60, v67
	v_mul_f32_e32 v61, v61, v67
	v_mul_f32_e32 v62, v62, v67
	v_mul_f32_e32 v63, v63, v67
	v_cvt_pk_bf16_f32 v76, v52, v53
	v_cvt_pk_bf16_f32 v77, v54, v55
	v_cvt_pk_bf16_f32 v78, v60, v61
	v_cvt_pk_bf16_f32 v79, v62, v63
	s_nop 1
	v_permlane16_swap_b32_e32 v76, v78
	v_permlane16_swap_b32_e32 v77, v79
	s_nop 1
	global_store_dwordx4 v71, v[76:79], s[58:59] offset:192
	s_barrier
